# s_setprio 1 during MLA MFMA segments and during diff softmax segments
# speedup vs baseline: 1.0341x; 1.0341x over previous
; #define SBAR() __builtin_amdgcn_sched_barrier(0)
; __device__ __forceinline__ void smax_tile(f32x16& p0, f32x16& p1, float& mhat, float& l_reg, f32x16 (&o)[4], float* al_l, const bool first, int r32, int hi,
;                                           bf16x8& pa0, bf16x8& pa1, bf16x8& pa2, bf16x8& pa3) {
;     ...
; #pragma unroll
;     for (int r = 0; r < 16; ++r) p0[r] = __builtin_amdgcn_exp2f(p0[r]);
; #pragma unroll
;     for (int r = 0; r < 16; ++r) p1[r] = __builtin_amdgcn_exp2f(p1[r]);
;     float ps = p0[0];
; #pragma unroll
;     for (int r = 1; r < 16; ++r) ps += p0[r];
; #pragma unroll
;     for (int r = 0; r < 16; ++r) ps += p1[r];
;     { auto rr = __builtin_amdgcn_permlane32_swap(__float_as_uint(ps), __float_as_uint(ps), false, false); ps = __uint_as_float(rr[0]) + __uint_as_float(rr[1]); }
;     l_reg += ps;
;     ...
;     PK4(p0, 0, pa0); PK4(p0, 8, pa1); PK4(p1, 0, pa2); PK4(p1, 8, pa3);
; template <int DQK, bool HASQK, bool HASPV, int J>
; __device__ __forceinline__ void slot_read(bf16x8 (&kf)[DQK / 16][2], s16x4 (&vf)[4][8], const int (&ka_)[4], int vb_) {
;     constexpr int NQS = HASQK ? 2 * (DQK / 16) : 0, NS = NQS + (HASPV ? 16 : 0);
;     if constexpr (J < NQS) { constexpr int d0 = J >> 1, h = J & 1; dsr128<(d0 >> 2) * 128 + h * 32 * DQK * 2>(kf[d0][h], ka_[d0 & 3]); }
;     else if constexpr (J < NS) { constexpr int q = J - NQS, g = q >> 2, d = q & 3; dstr64<v_rd_off(d, g, 0)>(vf[g][2 * d], vb_); dstr64<v_rd_off(d, g, 1)>(vf[g][2 * d + 1], vb_); }
; }
; template <int DQK, bool HASQK, bool HASPV, int J> ...
;     constexpr int NQS = HASQK ? 2 * (DQK / 16) : 0, NS = NQS + (HASPV ? 16 : 0);
;     if constexpr (J < NS) {
;         constexpr int rd1 = (J + 1 < NS) ? ((J + 1 < NQS) ? 1 : 2) : 0, rd2 = (J + 2 < NS) ? ((J + 2 < NQS) ? 1 : 2) : 0, rd3 = (J + 3 < NS) ? ((J + 3 < NQS) ? 1 : 2) : 0, NW = rd1 + rd2 + rd3;
;     ...
;         if constexpr (J < NQS) { constexpr int d0 = J >> 1, h = J & 1;
;             LWN1(kf[d0][h]); SBAR();
;             if constexpr (h == 0) p0 = __builtin_amdgcn_mfma_f32_32x32x16_bf16(kf[d0][0], qr[d0], (d0 == 0) ? negm : p0, 0, 0, 0);
;             else p1 = __builtin_amdgcn_mfma_f32_32x32x16_bf16(kf[d0][1], qr[d0], (d0 == 0) ? negm : p1, 0, 0, 0);
;         } else { constexpr int q = J - NQS, g = q >> 2, d = q & 3;
;             LWN2(vf[g][2 * d], vf[g][2 * d + 1]); SBAR();
.LBB0_605:
	v_exp_f32_e32 v96, v96
	v_exp_f32_e32 v97, v97
	v_exp_f32_e32 v98, v98
	v_exp_f32_e32 v99, v99
	v_exp_f32_e32 v100, v100
	v_exp_f32_e32 v101, v101
	v_add_f32_e32 v160, v96, v97
	v_exp_f32_e32 v102, v102
	v_add_f32_e32 v160, v98, v160
	v_exp_f32_e32 v103, v103
	v_add_f32_e32 v160, v99, v160
	v_exp_f32_e32 v104, v104
	v_add_f32_e32 v160, v100, v160
	v_exp_f32_e32 v105, v105
	v_add_f32_e32 v160, v101, v160
	v_exp_f32_e32 v106, v106
	v_add_f32_e32 v160, v102, v160
	v_exp_f32_e32 v107, v107
	v_add_f32_e32 v160, v103, v160
	v_exp_f32_e32 v108, v108
	v_add_f32_e32 v160, v104, v160
	v_exp_f32_e32 v109, v109
	v_add_f32_e32 v160, v105, v160
	v_exp_f32_e32 v110, v110
	v_add_f32_e32 v160, v106, v160
	v_exp_f32_e32 v111, v111
	v_add_f32_e32 v160, v107, v160
	v_exp_f32_e32 v80, v80
	v_add_f32_e32 v160, v108, v160
	v_exp_f32_e32 v81, v81
	v_add_f32_e32 v160, v109, v160
	v_exp_f32_e32 v82, v82
	v_add_f32_e32 v160, v110, v160
	v_exp_f32_e32 v83, v83
	v_add_f32_e32 v160, v111, v160
	v_exp_f32_e32 v84, v84
	v_add_f32_e32 v160, v80, v160
	v_exp_f32_e32 v85, v85
	v_add_f32_e32 v160, v81, v160
	v_exp_f32_e32 v86, v86
	v_add_f32_e32 v160, v82, v160
	v_exp_f32_e32 v87, v87
	v_add_f32_e32 v160, v83, v160
	v_exp_f32_e32 v88, v88
	v_add_f32_e32 v160, v84, v160
	v_exp_f32_e32 v89, v89
	v_add_f32_e32 v160, v85, v160
	v_exp_f32_e32 v90, v90
	v_add_f32_e32 v160, v86, v160
	v_exp_f32_e32 v91, v91
	v_add_f32_e32 v160, v87, v160
	v_exp_f32_e32 v92, v92
	v_add_f32_e32 v160, v88, v160
	v_exp_f32_e32 v93, v93
	v_add_f32_e32 v160, v89, v160
	v_exp_f32_e32 v94, v94
	v_add_f32_e32 v160, v90, v160
	v_exp_f32_e32 v95, v95
	v_add_f32_e32 v160, v91, v160
	v_add_f32_e32 v160, v92, v160
	v_add_f32_e32 v160, v93, v160
	v_add_f32_e32 v160, v94, v160
	v_add_f32_e32 v160, v95, v160
	v_mov_b32_e32 v161, v160
	s_nop 1
	v_permlane32_swap_b32_e32 v160, v161
	v_add_f32_e32 v160, v160, v161
	v_add_f32_e32 v204, v204, v160
	v_cvt_pk_bf16_f32 v172, v96, v97
	v_cvt_pk_bf16_f32 v173, v98, v99
	v_cvt_pk_bf16_f32 v174, v100, v101
	v_cvt_pk_bf16_f32 v175, v102, v103
	v_cvt_pk_bf16_f32 v168, v104, v105
	v_cvt_pk_bf16_f32 v169, v106, v107
	v_cvt_pk_bf16_f32 v170, v108, v109
	v_cvt_pk_bf16_f32 v171, v110, v111
	v_cvt_pk_bf16_f32 v164, v80, v81
	v_cvt_pk_bf16_f32 v165, v82, v83
	v_cvt_pk_bf16_f32 v166, v84, v85
	v_cvt_pk_bf16_f32 v167, v86, v87
	v_cvt_pk_bf16_f32 v160, v88, v89
	v_cvt_pk_bf16_f32 v161, v90, v91
	v_cvt_pk_bf16_f32 v162, v92, v93
	v_cvt_pk_bf16_f32 v163, v94, v95
	s_mul_i32 s47, s26, 0x6000
	s_waitcnt lgkmcnt(0)
	s_barrier
	s_setprio 1
	s_addk_i32 s93, 0xc000
	v_add_u32_e32 v207, s47, v185
	v_add_u32_e32 v224, s47, v187
	ds_read_b128 v[208:211], v207 offset:0
	ds_read_b128 v[212:215], v207 offset:0x3000
	ds_read_b128 v[216:219], v224 offset:0
	ds_read_b128 v[220:223], v224 offset:0x3000
	s_cmp_lg_u32 s26, 0
	s_cselect_b32 s46, s93, 0x8000
	v_xor_b32_e32 v80, 0x80000000, v203
	v_add_u32_e32 v225, s47, v205
	v_add_u32_e32 v226, s47, v206
	v_add_u32_e32 v227, s46, v202
	v_mov_b32_e32 v81, v80
	v_mov_b32_e32 v82, v80
	v_mov_b32_e32 v83, v80
	v_mov_b32_e32 v84, v80
	v_mov_b32_e32 v85, v80
	v_mov_b32_e32 v86, v80
	v_mov_b32_e32 v87, v80
	v_mov_b32_e32 v88, v80
	v_mov_b32_e32 v89, v80
	v_mov_b32_e32 v90, v80
	v_mov_b32_e32 v91, v80
	v_mov_b32_e32 v92, v80
	v_mov_b32_e32 v93, v80
	v_mov_b32_e32 v94, v80
	v_mov_b32_e32 v95, v80
	s_waitcnt lgkmcnt(3)
	s_nop 1
	v_mfma_f32_32x32x16_bf16 v[96:111], v[208:211], v[112:115], v[80:95]
	ds_read_b128 v[208:211], v225 offset:0
	s_waitcnt lgkmcnt(3)
	s_nop 0
	v_mfma_f32_32x32x16_bf16 v[80:95], v[212:215], v[112:115], v[80:95]
	ds_read_b128 v[212:215], v225 offset:0x3000
	s_waitcnt lgkmcnt(3)
	s_nop 0
	v_mfma_f32_32x32x16_bf16 v[96:111], v[216:219], v[116:119], v[96:111]
	ds_read_b128 v[216:219], v226 offset:0
	s_waitcnt lgkmcnt(3)
	s_nop 0
	v_mfma_f32_32x32x16_bf16 v[80:95], v[220:223], v[116:119], v[80:95]
	ds_read_b128 v[220:223], v226 offset:0x3000
	s_waitcnt lgkmcnt(3)
	s_nop 0
	v_mfma_f32_32x32x16_bf16 v[96:111], v[208:211], v[120:123], v[96:111]
	ds_read_b128 v[208:211], v207 offset:0x80
	s_waitcnt lgkmcnt(3)
	s_nop 0
	v_mfma_f32_32x32x16_bf16 v[80:95], v[212:215], v[120:123], v[80:95]
	ds_read_b128 v[212:215], v207 offset:0x3080
	s_waitcnt lgkmcnt(3)
	s_nop 0
	v_mfma_f32_32x32x16_bf16 v[96:111], v[216:219], v[124:127], v[96:111]
	ds_read_b128 v[216:219], v224 offset:0x80
	s_waitcnt lgkmcnt(3)
	s_nop 0
	v_mfma_f32_32x32x16_bf16 v[80:95], v[220:223], v[124:127], v[80:95]
	ds_read_b128 v[220:223], v224 offset:0x3080
	s_waitcnt lgkmcnt(3)
	s_nop 0
	v_mfma_f32_32x32x16_bf16 v[96:111], v[208:211], v[128:131], v[96:111]
	ds_read_b128 v[208:211], v225 offset:0x80
	s_waitcnt lgkmcnt(3)
	s_nop 0
	v_mfma_f32_32x32x16_bf16 v[80:95], v[212:215], v[128:131], v[80:95]
	ds_read_b128 v[212:215], v225 offset:0x3080
	s_waitcnt lgkmcnt(3)
	s_nop 0
	v_mfma_f32_32x32x16_bf16 v[96:111], v[216:219], v[132:135], v[96:111]
	ds_read_b128 v[216:219], v226 offset:0x80
	s_waitcnt lgkmcnt(3)
	s_nop 0
	v_mfma_f32_32x32x16_bf16 v[80:95], v[220:223], v[132:135], v[80:95]
	ds_read_b128 v[220:223], v226 offset:0x3080
	s_waitcnt lgkmcnt(3)
; template <int DQK, bool HASQK, bool HASPV, int J>
; __device__ __forceinline__ void slot_read(bf16x8 (&kf)[DQK / 16][2], s16x4 (&vf)[4][8], const int (&ka_)[4], int vb_) {
;     constexpr int NQS = HASQK ? 2 * (DQK / 16) : 0, NS = NQS + (HASPV ? 16 : 0);
;     if constexpr (J < NQS) { constexpr int d0 = J >> 1, h = J & 1; dsr128<(d0 >> 2) * 128 + h * 32 * DQK * 2>(kf[d0][h], ka_[d0 & 3]); }
;     else if constexpr (J < NS) { constexpr int q = J - NQS, g = q >> 2, d = q & 3; dstr64<v_rd_off(d, g, 0)>(vf[g][2 * d], vb_); dstr64<v_rd_off(d, g, 1)>(vf[g][2 * d + 1], vb_); }
; }
; template <int DQK, bool HASQK, bool HASPV, int J> ...
;     constexpr int NQS = HASQK ? 2 * (DQK / 16) : 0, NS = NQS + (HASPV ? 16 : 0);
;     if constexpr (J < NS) {
;         constexpr int rd1 = (J + 1 < NS) ? ((J + 1 < NQS) ? 1 : 2) : 0, rd2 = (J + 2 < NS) ? ((J + 2 < NQS) ? 1 : 2) : 0, rd3 = (J + 3 < NS) ? ((J + 3 < NQS) ? 1 : 2) : 0, NW = rd1 + rd2 + rd3;
;     ...
;         if constexpr (J < NQS) { constexpr int d0 = J >> 1, h = J & 1;
;             LWN1(kf[d0][h]); SBAR();
;             if constexpr (h == 0) p0 = __builtin_amdgcn_mfma_f32_32x32x16_bf16(kf[d0][0], qr[d0], (d0 == 0) ? negm : p0, 0, 0, 0);
;             else p1 = __builtin_amdgcn_mfma_f32_32x32x16_bf16(kf[d0][1], qr[d0], (d0 == 0) ? negm : p1, 0, 0, 0);
;         } else { constexpr int q = J - NQS, g = q >> 2, d = q & 3;
;             LWN2(vf[g][2 * d], vf[g][2 * d + 1]); SBAR();
;             o[d] = __builtin_amdgcn_mfma_f32_32x32x16_bf16(pa[g], (bf16x8){vf[g][2 * d][0], vf[g][2 * d][1], vf[g][2 * d][2], vf[g][2 * d][3], vf[g][2 * d + 1][0], vf[g][2 * d + 1][1], vf[g][2 * d + 1][2], vf[g][2 * d + 1][3]}, o[d], 0, 0, 0);
;         }
;     ...
;         SBAR();
;         slot_read<DQK, HASQK, HASPV, J + 4>(kf, vf, ka_, vb_);
;         SBAR();
;         slot_run<DQK, HASQK, HASPV, J + 1>(kf, vf, ka_, vb_, qr, p0, p1, negm, o, pa);
;     }
; }
;     ...
;     for (int i = 0; i < NT - 1; ++i) {
;         SEG_S(i);
;         { const int cp = (ci == 0) ? 2 : ci - 1, cn = (ci == 2) ? 0 : ci + 1;
;           if (DMA_M) { if (i + 3 < NT) DMA_K(i + 3, cp); if (i + 2 < NT) DMA_V(i + 2, cn); }
;           SEG_M(true, true, ci, cp);
;           if (DMA_M && i + 3 < NT) asm volatile("s_waitcnt vmcnt(%0)" :: "n"(NKW + 2) : "memory");
;           else asm volatile("s_waitcnt vmcnt(0)" ::: "memory");
;           BAR_ALL(); }
	s_nop 0
	v_mfma_f32_32x32x16_bf16 v[96:111], v[208:211], v[136:139], v[96:111]
	ds_read_b128 v[208:211], v207 offset:0x100
	s_waitcnt lgkmcnt(3)
	s_nop 0
	v_mfma_f32_32x32x16_bf16 v[80:95], v[212:215], v[136:139], v[80:95]
	ds_read_b128 v[212:215], v207 offset:0x3100
	s_waitcnt lgkmcnt(3)
	s_nop 0
	v_mfma_f32_32x32x16_bf16 v[96:111], v[216:219], v[140:143], v[96:111]
	ds_read_b128 v[216:219], v224 offset:0x100
	s_waitcnt lgkmcnt(3)
	s_nop 0
	v_mfma_f32_32x32x16_bf16 v[80:95], v[220:223], v[140:143], v[80:95]
	ds_read_b128 v[220:223], v224 offset:0x3100
	s_waitcnt lgkmcnt(3)
	s_nop 0
	v_mfma_f32_32x32x16_bf16 v[96:111], v[208:211], v[144:147], v[96:111]
	ds_read_b128 v[208:211], v225 offset:0x100
	s_waitcnt lgkmcnt(3)
	s_nop 0
	v_mfma_f32_32x32x16_bf16 v[80:95], v[212:215], v[144:147], v[80:95]
	ds_read_b128 v[212:215], v225 offset:0x3100
	s_waitcnt lgkmcnt(3)
	s_nop 0
	v_mfma_f32_32x32x16_bf16 v[96:111], v[216:219], v[148:151], v[96:111]
	ds_read_b128 v[216:219], v226 offset:0x100
	s_waitcnt lgkmcnt(3)
	s_nop 0
	v_mfma_f32_32x32x16_bf16 v[80:95], v[220:223], v[148:151], v[80:95]
	ds_read_b128 v[220:223], v226 offset:0x3100
	s_waitcnt lgkmcnt(3)
	s_nop 0
	v_mfma_f32_32x32x16_bf16 v[96:111], v[208:211], v[152:155], v[96:111]
	ds_read_b64_tr_b16 v[208:209], v227 offset:0
	ds_read_b64_tr_b16 v[210:211], v227 offset:0x800
	s_waitcnt lgkmcnt(4)
	s_nop 0
	v_mfma_f32_32x32x16_bf16 v[80:95], v[212:215], v[152:155], v[80:95]
	ds_read_b64_tr_b16 v[212:213], v227 offset:0x200
	ds_read_b64_tr_b16 v[214:215], v227 offset:0xa00
	s_waitcnt lgkmcnt(5)
	s_nop 0
	v_mfma_f32_32x32x16_bf16 v[96:111], v[216:219], v[156:159], v[96:111]
	ds_read_b64_tr_b16 v[216:217], v227 offset:0x400
	ds_read_b64_tr_b16 v[218:219], v227 offset:0xc00
	s_waitcnt lgkmcnt(6)
	s_nop 0
	v_mfma_f32_32x32x16_bf16 v[80:95], v[220:223], v[156:159], v[80:95]
	ds_read_b64_tr_b16 v[220:221], v227 offset:0x600
	ds_read_b64_tr_b16 v[222:223], v227 offset:0xe00
	s_waitcnt lgkmcnt(6)
	s_nop 0
	v_mfma_f32_32x32x16_bf16 v[64:79], v[172:175], v[208:211], v[64:79]
	ds_read_b64_tr_b16 v[208:209], v227 offset:0x1000
	ds_read_b64_tr_b16 v[210:211], v227 offset:0x1800
	s_waitcnt lgkmcnt(6)
	s_nop 0
	v_mfma_f32_32x32x16_bf16 v[48:63], v[172:175], v[212:215], v[48:63]
	ds_read_b64_tr_b16 v[212:213], v227 offset:0x1200
	ds_read_b64_tr_b16 v[214:215], v227 offset:0x1a00
	s_waitcnt lgkmcnt(6)
	s_nop 0
	v_mfma_f32_32x32x16_bf16 v[32:47], v[172:175], v[216:219], v[32:47]
	ds_read_b64_tr_b16 v[216:217], v227 offset:0x1400
	ds_read_b64_tr_b16 v[218:219], v227 offset:0x1c00
	s_waitcnt lgkmcnt(6)
	s_nop 0
	v_mfma_f32_32x32x16_bf16 v[16:31], v[172:175], v[220:223], v[16:31]
	ds_read_b64_tr_b16 v[172:173], v227 offset:0x1600
	ds_read_b64_tr_b16 v[174:175], v227 offset:0x1e00
	s_waitcnt lgkmcnt(6)
	s_nop 0
	v_mfma_f32_32x32x16_bf16 v[64:79], v[168:171], v[208:211], v[64:79]
	ds_read_b64_tr_b16 v[208:209], v227 offset:0x2000
	ds_read_b64_tr_b16 v[210:211], v227 offset:0x2800
	s_waitcnt lgkmcnt(6)
	s_nop 0
	v_mfma_f32_32x32x16_bf16 v[48:63], v[168:171], v[212:215], v[48:63]
	ds_read_b64_tr_b16 v[212:213], v227 offset:0x2200
	ds_read_b64_tr_b16 v[214:215], v227 offset:0x2a00
	s_waitcnt lgkmcnt(6)
	s_nop 0
	v_mfma_f32_32x32x16_bf16 v[32:47], v[168:171], v[216:219], v[32:47]
	ds_read_b64_tr_b16 v[216:217], v227 offset:0x2400
	ds_read_b64_tr_b16 v[218:219], v227 offset:0x2c00
	s_waitcnt lgkmcnt(6)
	s_nop 0
	v_mfma_f32_32x32x16_bf16 v[16:31], v[168:171], v[172:175], v[16:31]
	ds_read_b64_tr_b16 v[168:169], v227 offset:0x2600
	ds_read_b64_tr_b16 v[170:171], v227 offset:0x2e00
	s_waitcnt lgkmcnt(6)
	s_nop 0
	v_mfma_f32_32x32x16_bf16 v[64:79], v[164:167], v[208:211], v[64:79]
	ds_read_b64_tr_b16 v[172:173], v227 offset:0x3000
	ds_read_b64_tr_b16 v[174:175], v227 offset:0x3800
	s_waitcnt lgkmcnt(6)
	s_nop 0
	v_mfma_f32_32x32x16_bf16 v[48:63], v[164:167], v[212:215], v[48:63]
	ds_read_b64_tr_b16 v[208:209], v227 offset:0x3200
	ds_read_b64_tr_b16 v[210:211], v227 offset:0x3a00
	s_waitcnt lgkmcnt(6)
	s_nop 0
	v_mfma_f32_32x32x16_bf16 v[32:47], v[164:167], v[216:219], v[32:47]
	ds_read_b64_tr_b16 v[212:213], v227 offset:0x3400
	ds_read_b64_tr_b16 v[214:215], v227 offset:0x3c00
	s_waitcnt lgkmcnt(6)
	s_nop 0
	v_mfma_f32_32x32x16_bf16 v[16:31], v[164:167], v[168:171], v[16:31]
	ds_read_b64_tr_b16 v[164:165], v227 offset:0x3600
	ds_read_b64_tr_b16 v[166:167], v227 offset:0x3e00
	s_waitcnt lgkmcnt(6)
	s_nop 0
	v_mfma_f32_32x32x16_bf16 v[64:79], v[160:163], v[172:175], v[64:79]
	s_waitcnt lgkmcnt(4)
	s_nop 0
	v_mfma_f32_32x32x16_bf16 v[48:63], v[160:163], v[208:211], v[48:63]
	s_waitcnt lgkmcnt(2)
	s_nop 0
	v_mfma_f32_32x32x16_bf16 v[32:47], v[160:163], v[212:215], v[32:47]
	s_waitcnt lgkmcnt(0)
	s_nop 0
	v_mfma_f32_32x32x16_bf16 v[16:31], v[160:163], v[164:167], v[16:31]
	s_setprio 0
	s_waitcnt vmcnt(0)
	s_waitcnt lgkmcnt(0)
	s_barrier
	s_add_u32 s44, s44, 0x18000
	s_addc_u32 s45, s45, 0
	v_lshl_add_u64 v[194:195], v[194:195], 0, s[28:29]
	s_cmp_eq_u32 s44, 0xbe8000
	v_lshl_add_u64 v[196:197], v[196:197], 0, s[28:29]
	s_cbranch_scc1 .LBB0_616

; #define PK4(P, BASE, OUT) do { u32x4 w = {cvtpk(P[BASE + 0], P[BASE + 1]), cvtpk(P[BASE + 2], P[BASE + 3]), cvtpk(P[BASE + 4], P[BASE + 5]), cvtpk(P[BASE + 6], P[BASE + 7])}; \
;     OUT = *reinterpret_cast<bf16x8*>(&w); } while (0)
; __device__ __forceinline__ void smax_tile(f32x16& p0, f32x16& p1, float& mhat, float& l_reg, f32x16 (&o)[4], float* al_l, const bool first, int r32, int hi,
;                                           bf16x8& pa0, bf16x8& pa1, bf16x8& pa2, bf16x8& pa3) {
;     ...
; #pragma unroll
;     for (int r = 0; r < 16; ++r) p0[r] = __builtin_amdgcn_exp2f(p0[r]);
; #pragma unroll
;     for (int r = 0; r < 16; ++r) p1[r] = __builtin_amdgcn_exp2f(p1[r]);
;     float ps = p0[0];
; #pragma unroll
;     for (int r = 1; r < 16; ++r) ps += p0[r];
; #pragma unroll
;     for (int r = 0; r < 16; ++r) ps += p1[r];
;     { auto rr = __builtin_amdgcn_permlane32_swap(__float_as_uint(ps), __float_as_uint(ps), false, false); ps = __uint_as_float(rr[0]) + __uint_as_float(rr[1]); }
;     l_reg += ps;
;     ...
;     PK4(p0, 0, pa0); PK4(p0, 8, pa1); PK4(p1, 0, pa2); PK4(p1, 8, pa3);
.LBB0_651:
	v_exp_f32_e32 v96, v96
	v_exp_f32_e32 v97, v97
	v_exp_f32_e32 v98, v98
	v_exp_f32_e32 v99, v99
	v_exp_f32_e32 v100, v100
	v_exp_f32_e32 v101, v101
	v_add_f32_e32 v128, v96, v97
	v_exp_f32_e32 v102, v102
	v_add_f32_e32 v128, v98, v128
	v_exp_f32_e32 v103, v103
	v_add_f32_e32 v128, v99, v128
	v_exp_f32_e32 v104, v104
	v_add_f32_e32 v128, v100, v128
	v_exp_f32_e32 v105, v105
	v_add_f32_e32 v128, v101, v128
	v_exp_f32_e32 v106, v106
	v_add_f32_e32 v128, v102, v128
	v_exp_f32_e32 v107, v107
	v_add_f32_e32 v128, v103, v128
	v_exp_f32_e32 v108, v108
	v_add_f32_e32 v128, v104, v128
	v_exp_f32_e32 v109, v109
	v_add_f32_e32 v128, v105, v128
	v_exp_f32_e32 v110, v110
	v_add_f32_e32 v128, v106, v128
	v_exp_f32_e32 v111, v111
	v_add_f32_e32 v128, v107, v128
	v_exp_f32_e32 v80, v80
	v_add_f32_e32 v128, v108, v128
	v_exp_f32_e32 v81, v81
	v_add_f32_e32 v128, v109, v128
	v_exp_f32_e32 v82, v82
	v_add_f32_e32 v128, v110, v128
	v_exp_f32_e32 v83, v83
	v_add_f32_e32 v128, v111, v128
	v_exp_f32_e32 v84, v84
	v_add_f32_e32 v128, v80, v128
	v_exp_f32_e32 v85, v85
	v_add_f32_e32 v128, v81, v128
	v_exp_f32_e32 v86, v86
	v_add_f32_e32 v128, v82, v128
	v_exp_f32_e32 v87, v87
	v_add_f32_e32 v128, v83, v128
	v_exp_f32_e32 v88, v88
	v_add_f32_e32 v128, v84, v128
	v_exp_f32_e32 v89, v89
	v_add_f32_e32 v128, v85, v128
	v_exp_f32_e32 v90, v90
	v_add_f32_e32 v128, v86, v128
	v_exp_f32_e32 v91, v91
	v_add_f32_e32 v128, v87, v128
	v_exp_f32_e32 v92, v92
	v_add_f32_e32 v128, v88, v128
	v_exp_f32_e32 v93, v93
	v_add_f32_e32 v128, v89, v128
	v_exp_f32_e32 v94, v94
	v_add_f32_e32 v128, v90, v128
	v_exp_f32_e32 v95, v95
	v_add_f32_e32 v128, v91, v128
	v_add_f32_e32 v128, v92, v128
	v_add_f32_e32 v128, v93, v128
	v_add_f32_e32 v128, v94, v128
	v_add_f32_e32 v128, v95, v128
	v_mov_b32_e32 v129, v128
	s_nop 1
	v_permlane32_swap_b32_e32 v128, v129
	v_add_f32_e32 v128, v128, v129
	s_addk_i32 s87, 0xc000
	v_add_f32_e32 v159, v159, v128
	v_cvt_pk_bf16_f32 v162, v96, v97
	v_cvt_pk_bf16_f32 v163, v98, v99
	v_cvt_pk_bf16_f32 v164, v100, v101
	v_cvt_pk_bf16_f32 v165, v102, v103
	v_cvt_pk_bf16_f32 v166, v104, v105
	v_cvt_pk_bf16_f32 v167, v106, v107
	v_cvt_pk_bf16_f32 v168, v108, v109
	v_cvt_pk_bf16_f32 v169, v110, v111
	v_cvt_pk_bf16_f32 v132, v80, v81
	v_cvt_pk_bf16_f32 v133, v82, v83
	v_cvt_pk_bf16_f32 v134, v84, v85
	v_cvt_pk_bf16_f32 v135, v86, v87
	v_cvt_pk_bf16_f32 v128, v88, v89
	v_cvt_pk_bf16_f32 v129, v90, v91
	v_cvt_pk_bf16_f32 v130, v92, v93
	v_cvt_pk_bf16_f32 v131, v94, v95
	s_cmp_lg_u32 s86, 0
	s_setprio 0
	s_waitcnt lgkmcnt(0)
	s_barrier
; #define SBAR() __builtin_amdgcn_sched_barrier(0)
; template <int OFF> __device__ __forceinline__ void dsr128(bf16x8& d, int addr) { asm volatile("ds_read_b128 %0, %1 offset:%2" : "=v"(d) : "v"(addr), "i"(OFF)); }
; template <int OFF> __device__ __forceinline__ void dstr64(s16x4& d, int addr) { asm volatile("ds_read_b64_tr_b16 %0, %1 offset:%2" : "=v"(d) : "v"(addr), "i"(OFF)); }
; template <int DQK, bool HASQK, bool HASPV, int J>
; __device__ __forceinline__ void slot_read(bf16x8 (&kf)[DQK / 16][2], s16x4 (&vf)[4][8], const int (&ka_)[4], int vb_) {
;     constexpr int NQS = HASQK ? 2 * (DQK / 16) : 0, NS = NQS + (HASPV ? 16 : 0);
;     if constexpr (J < NQS) { constexpr int d0 = J >> 1, h = J & 1; dsr128<(d0 >> 2) * 128 + h * 32 * DQK * 2>(kf[d0][h], ka_[d0 & 3]); }
;     else if constexpr (J < NS) { constexpr int q = J - NQS, g = q >> 2, d = q & 3; dstr64<v_rd_off(d, g, 0)>(vf[g][2 * d], vb_); dstr64<v_rd_off(d, g, 1)>(vf[g][2 * d + 1], vb_); }
; }
; template <int DQK, bool HASQK, bool HASPV, int J> ...
;     constexpr int NQS = HASQK ? 2 * (DQK / 16) : 0, NS = NQS + (HASPV ? 16 : 0);
;     if constexpr (J < NS) {
;         constexpr int rd1 = (J + 1 < NS) ? ((J + 1 < NQS) ? 1 : 2) : 0, rd2 = (J + 2 < NS) ? ((J + 2 < NQS) ? 1 : 2) : 0, rd3 = (J + 3 < NS) ? ((J + 3 < NQS) ? 1 : 2) : 0, NW = rd1 + rd2 + rd3;
;     ...
;         if constexpr (J < NQS) { constexpr int d0 = J >> 1, h = J & 1;
;             LWN1(kf[d0][h]); SBAR();
;             if constexpr (h == 0) p0 = __builtin_amdgcn_mfma_f32_32x32x16_bf16(kf[d0][0], qr[d0], (d0 == 0) ? negm : p0, 0, 0, 0);
;             else p1 = __builtin_amdgcn_mfma_f32_32x32x16_bf16(kf[d0][1], qr[d0], (d0 == 0) ? negm : p1, 0, 0, 0);
;         } else { constexpr int q = J - NQS, g = q >> 2, d = q & 3;
;             LWN2(vf[g][2 * d], vf[g][2 * d + 1]); SBAR();
;             o[d] = __builtin_amdgcn_mfma_f32_32x32x16_bf16(pa[g], (bf16x8){vf[g][2 * d][0], vf[g][2 * d][1], vf[g][2 * d][2], vf[g][2 * d][3], vf[g][2 * d + 1][0], vf[g][2 * d + 1][1], vf[g][2 * d + 1][2], vf[g][2 * d + 1][3]}, o[d], 0, 0, 0);
;         }
;     ...
;         SBAR();
;         slot_read<DQK, HASQK, HASPV, J + 4>(kf, vf, ka_, vb_);
;         SBAR();
;         slot_run<DQK, HASQK, HASPV, J + 1>(kf, vf, ka_, vb_, qr, p0, p1, negm, o, pa);
;     }
; }
	s_cselect_b32 s46, s87, 0x8000
	s_lshl_b32 s47, s86, 13
	v_add_u32_e32 v81, s47, v141
	v_add_u32_e32 v82, s47, v143
	ds_read_b128 v[170:173], v81 offset:0
	ds_read_b128 v[174:177], v81 offset:0x1000
	ds_read_b128 v[178:181], v82 offset:0
	ds_read_b128 v[182:185], v82 offset:0x1000
	v_xor_b32_e32 v80, 0x80000000, v158
	v_add_u32_e32 v186, s47, v160
	v_add_u32_e32 v187, s47, v161
	v_add_u32_e32 v188, s46, v157
	v_mov_b32_e32 v81, v80
	v_mov_b32_e32 v82, v80
	v_mov_b32_e32 v83, v80
	v_mov_b32_e32 v84, v80
	v_mov_b32_e32 v85, v80
	v_mov_b32_e32 v86, v80
	v_mov_b32_e32 v87, v80
	v_mov_b32_e32 v88, v80
	v_mov_b32_e32 v89, v80
	v_mov_b32_e32 v90, v80
	v_mov_b32_e32 v91, v80
	v_mov_b32_e32 v92, v80
	v_mov_b32_e32 v93, v80
	v_mov_b32_e32 v94, v80
	v_mov_b32_e32 v95, v80
	s_waitcnt lgkmcnt(3)
	s_nop 1
	v_mfma_f32_32x32x16_bf16 v[96:111], v[170:173], v[112:115], v[80:95]
	ds_read_b128 v[170:173], v186 offset:0
	s_waitcnt lgkmcnt(3)
	s_nop 0
	v_mfma_f32_32x32x16_bf16 v[80:95], v[174:177], v[112:115], v[80:95]
	ds_read_b128 v[174:177], v186 offset:0x1000
	s_waitcnt lgkmcnt(3)
	s_nop 0
	v_mfma_f32_32x32x16_bf16 v[96:111], v[178:181], v[116:119], v[96:111]
	ds_read_b128 v[178:181], v187 offset:0
	s_waitcnt lgkmcnt(3)
	s_nop 0
	v_mfma_f32_32x32x16_bf16 v[80:95], v[182:185], v[116:119], v[80:95]
	ds_read_b128 v[182:185], v187 offset:0x1000
	s_waitcnt lgkmcnt(3)
	s_nop 0
	v_mfma_f32_32x32x16_bf16 v[96:111], v[170:173], v[120:123], v[96:111]
	ds_read_b64_tr_b16 v[170:171], v188 offset:0
	ds_read_b64_tr_b16 v[172:173], v188 offset:0x800
	s_waitcnt lgkmcnt(4)
	s_nop 0
	v_mfma_f32_32x32x16_bf16 v[80:95], v[174:177], v[120:123], v[80:95]
	ds_read_b64_tr_b16 v[174:175], v188 offset:0x200
	ds_read_b64_tr_b16 v[176:177], v188 offset:0xa00
	s_waitcnt lgkmcnt(5)
	s_nop 0
	v_mfma_f32_32x32x16_bf16 v[96:111], v[178:181], v[124:127], v[96:111]
	ds_read_b64_tr_b16 v[178:179], v188 offset:0x400
	ds_read_b64_tr_b16 v[180:181], v188 offset:0xc00
	s_waitcnt lgkmcnt(6)
	s_nop 0
	v_mfma_f32_32x32x16_bf16 v[80:95], v[182:185], v[124:127], v[80:95]
	ds_read_b64_tr_b16 v[182:183], v188 offset:0x600
	ds_read_b64_tr_b16 v[184:185], v188 offset:0xe00
	s_waitcnt lgkmcnt(6)
	s_nop 0
	v_mfma_f32_32x32x16_bf16 v[64:79], v[162:165], v[170:173], v[64:79]
	ds_read_b64_tr_b16 v[170:171], v188 offset:0x1000
	ds_read_b64_tr_b16 v[172:173], v188 offset:0x1800
	s_waitcnt lgkmcnt(6)
	s_nop 0
	v_mfma_f32_32x32x16_bf16 v[48:63], v[162:165], v[174:177], v[48:63]
	ds_read_b64_tr_b16 v[174:175], v188 offset:0x1200
	ds_read_b64_tr_b16 v[176:177], v188 offset:0x1a00
	s_waitcnt lgkmcnt(6)
	s_nop 0
	v_mfma_f32_32x32x16_bf16 v[32:47], v[162:165], v[178:181], v[32:47]
	ds_read_b64_tr_b16 v[178:179], v188 offset:0x1400
	ds_read_b64_tr_b16 v[180:181], v188 offset:0x1c00
	s_waitcnt lgkmcnt(6)
	s_nop 0
	v_mfma_f32_32x32x16_bf16 v[16:31], v[162:165], v[182:185], v[16:31]
	ds_read_b64_tr_b16 v[162:163], v188 offset:0x1600
	ds_read_b64_tr_b16 v[164:165], v188 offset:0x1e00
	s_waitcnt lgkmcnt(6)
	s_nop 0
	v_mfma_f32_32x32x16_bf16 v[64:79], v[166:169], v[170:173], v[64:79]
	ds_read_b64_tr_b16 v[170:171], v188 offset:0x2000
	ds_read_b64_tr_b16 v[172:173], v188 offset:0x2800
	s_waitcnt lgkmcnt(6)
	s_nop 0
	v_mfma_f32_32x32x16_bf16 v[48:63], v[166:169], v[174:177], v[48:63]
	ds_read_b64_tr_b16 v[174:175], v188 offset:0x2200
	ds_read_b64_tr_b16 v[176:177], v188 offset:0x2a00
	s_waitcnt lgkmcnt(6)
	s_nop 0
	v_mfma_f32_32x32x16_bf16 v[32:47], v[166:169], v[178:181], v[32:47]
	ds_read_b64_tr_b16 v[178:179], v188 offset:0x2400
	ds_read_b64_tr_b16 v[180:181], v188 offset:0x2c00
	s_waitcnt lgkmcnt(6)
	s_nop 0
	v_mfma_f32_32x32x16_bf16 v[16:31], v[166:169], v[162:165], v[16:31]
	ds_read_b64_tr_b16 v[162:163], v188 offset:0x2600
	ds_read_b64_tr_b16 v[164:165], v188 offset:0x2e00
	s_waitcnt lgkmcnt(6)
	s_nop 0
	v_mfma_f32_32x32x16_bf16 v[64:79], v[132:135], v[170:173], v[64:79]
	ds_read_b64_tr_b16 v[166:167], v188 offset:0x3000
	ds_read_b64_tr_b16 v[168:169], v188 offset:0x3800
	s_waitcnt lgkmcnt(6)
	s_nop 0
	v_mfma_f32_32x32x16_bf16 v[48:63], v[132:135], v[174:177], v[48:63]
	ds_read_b64_tr_b16 v[170:171], v188 offset:0x3200
	ds_read_b64_tr_b16 v[172:173], v188 offset:0x3a00
	s_waitcnt lgkmcnt(6)
	s_nop 0
	v_mfma_f32_32x32x16_bf16 v[32:47], v[132:135], v[178:181], v[32:47]
	ds_read_b64_tr_b16 v[174:175], v188 offset:0x3400
	ds_read_b64_tr_b16 v[176:177], v188 offset:0x3c00
	s_waitcnt lgkmcnt(6)
	s_nop 0
	v_mfma_f32_32x32x16_bf16 v[16:31], v[132:135], v[162:165], v[16:31]
	ds_read_b64_tr_b16 v[132:133], v188 offset:0x3600
	ds_read_b64_tr_b16 v[134:135], v188 offset:0x3e00
	s_waitcnt lgkmcnt(6)
	s_nop 0
	v_mfma_f32_32x32x16_bf16 v[64:79], v[128:131], v[166:169], v[64:79]
	s_waitcnt lgkmcnt(4)
	s_nop 0
	v_mfma_f32_32x32x16_bf16 v[48:63], v[128:131], v[170:173], v[48:63]
	s_waitcnt lgkmcnt(2)
	s_nop 0
	v_mfma_f32_32x32x16_bf16 v[32:47], v[128:131], v[174:177], v[32:47]
	s_waitcnt lgkmcnt(0)
	s_nop 0
	v_mfma_f32_32x32x16_bf16 v[16:31], v[128:131], v[132:135], v[16:31]
	s_waitcnt vmcnt(0)
	s_add_u32 s44, s44, 0x10000
	s_waitcnt lgkmcnt(0)
	s_barrier
	s_addc_u32 s45, s45, 0
	s_cmp_eq_u32 s44, 0x7f0000
	s_cbranch_scc1 .LBB0_662
.LBB0_652:
	s_setprio 1
	s_cmp_eq_u32 s44, 0x7e0000
	s_cbranch_scc1 .LBB0_654
	s_lshl_b32 s46, s86, 13
	s_addk_i32 s46, 0xe000
	s_cmp_lg_u32 s86, 0
	s_cselect_b32 s46, s46, 0x4000
	v_lshl_add_u64 v[128:129], v[144:145], 0, s[44:45]
	s_add_i32 m0, s69, s46
	s_nop 0
	global_load_lds_dwordx4 v[128:129], off
